# v031 + waiting workgroups keep two staggered polls of the release word in flight
# speedup vs baseline: 1.0185x; 1.0011x over previous
; __device__ __forceinline__ unsigned xb_ld(unsigned* p)              { return __hip_atomic_load(p, __ATOMIC_RELAXED, __HIP_MEMORY_SCOPE_AGENT); }
; __device__ __forceinline__ unsigned xb_add(unsigned* p, unsigned v) { return __hip_atomic_fetch_add(p, v, __ATOMIC_RELAXED, __HIP_MEMORY_SCOPE_AGENT); }
; #define XB_SPIN(cond, bar) do { unsigned _sp = 0; while (cond) { __builtin_amdgcn_s_sleep(1); \
;     if ((++_sp & 255u) == 0u) { if (xb_ld(&(bar)[XB_TMO])) break; if (_sp > XB_SPIN_CAP) { atomicAdd(&(bar)[XB_TMO], 1u); break; } } } } while (0)
; __device__ __forceinline__ void xcd_barrier(const XcdBarrier& b) {
;     ...
;         const unsigned old = xb_add(&bar[XB_XSUB(b.x)], 1u);
;         const unsigned gen = old / nloc;
;         if (old + 1u == (gen + 1u) * nloc) {
;             __builtin_amdgcn_fence(__ATOMIC_RELEASE, "agent");
;             asm volatile("s_waitcnt vmcnt(0)" ::: "memory");
;             const unsigned og = xb_add(&bar[XB_TOP], 1u);
;             const unsigned tg = og / nx;
;             if (og + 1u == (tg + 1u) * nx) xb_add(&bar[XB_TOPGEN], 1u);
;             else XB_SPIN(xb_ld(&bar[XB_TOPGEN]) == tg, bar);
;             __builtin_amdgcn_fence(__ATOMIC_ACQUIRE, "agent");
;             xb_add(&bar[XB_XGEN(b.x)], 1u);
;             asm volatile("s_waitcnt vmcnt(0)" ::: "memory");
;         } else {
;             XB_SPIN(xb_ld(&bar[XB_XGEN(b.x)]) == gen, bar);
;             __builtin_amdgcn_fence(__ATOMIC_ACQUIRE, "agent");
;             asm volatile("s_waitcnt vmcnt(0)" ::: "memory");
.LBB0_301:
	s_or_b64 exec, exec, s[6:7]
	v_cvt_f32_u32_e32 v5, v3
	s_waitcnt vmcnt(0)
	buffer_inv sc1
	v_readfirstlane_b32 s5, v4
	v_sub_u32_e32 v4, 0, v3
	v_rcp_iflag_f32_e32 v5, v5
	v_add_u32_e32 v6, s5, v1
	v_mul_f32_e32 v5, 0x4f7ffffe, v5
	v_cvt_u32_f32_e32 v5, v5
	v_mul_lo_u32 v1, v4, v5
	v_mul_hi_u32 v1, v5, v1
	v_add_u32_e32 v1, v5, v1
	v_mul_hi_u32 v1, v6, v1
	v_mul_lo_u32 v4, v1, v3
	v_sub_u32_e32 v4, v6, v4
	v_add_u32_e32 v5, 1, v1
	v_cmp_ge_u32_e32 vcc, v4, v3
	s_nop 1
	v_cndmask_b32_e32 v1, v1, v5, vcc
	v_sub_u32_e32 v5, v4, v3
	v_cndmask_b32_e32 v4, v4, v5, vcc
	v_add_u32_e32 v5, 1, v1
	v_cmp_ge_u32_e32 vcc, v4, v3
	v_add_u32_e32 v4, 1, v6
	s_nop 0
	v_cndmask_b32_e32 v1, v1, v5, vcc
	v_mul_lo_u32 v5, v3, v1
	v_add_u32_e32 v3, v5, v3
	v_cmp_ne_u32_e32 vcc, v4, v3
	s_waitcnt lgkmcnt(0)
	v_add_u32_e32 v16, -1, v1
	v_mul_lo_u32 v16, v16, v2
	s_and_saveexec_b64 s[6:7], vcc
	s_xor_b64 s[6:7], exec, s[6:7]
	s_cbranch_execz .LBB0_315
	v_readlane_b32 s8, v253, 48
	v_readlane_b32 s9, v253, 49
	s_waitcnt lgkmcnt(0)
	s_nop 3
	s_add_u32 s8, s8, 0x3600
	s_addc_u32 s9, s9, 0
	s_mov_b32 s20, 0
	global_load_dword v2, v163, s[8:9] sc1
	s_sleep 10
.Lbar_nl_poll_12:
	global_load_dword v3, v163, s[8:9] sc1
	s_waitcnt vmcnt(1)
	v_cmp_le_u32_e32 vcc, v16, v2
	s_cbranch_vccnz .Lbar_nl_done_12
	global_load_dword v2, v163, s[8:9] sc1
	s_waitcnt vmcnt(1)
	v_cmp_le_u32_e32 vcc, v16, v3
	s_cbranch_vccnz .Lbar_nl_done_12
	s_add_i32 s20, s20, 1
	s_cmp_lt_u32 s20, 0x20000
	s_cbranch_scc1 .Lbar_nl_poll_12
.Lbar_nl_done_12:
	s_waitcnt vmcnt(0)
.LBB0_315:
	s_andn2_saveexec_b64 s[6:7], s[6:7]
	s_cbranch_execz .LBB0_335
	s_mov_b64 s[6:7], exec
	buffer_wbl2 sc1
	s_waitcnt lgkmcnt(0)
	s_waitcnt vmcnt(0)
	v_readlane_b32 s18, v253, 48
	v_readlane_b32 s19, v253, 49
	v_readlane_b32 s12, v253, 52
	v_readlane_b32 s13, v253, 53
	s_nop 3
	s_add_u32 s18, s18, 0x3600
	s_addc_u32 s19, s19, 0
	s_add_u32 s12, s12, 0x2500
	s_addc_u32 s13, s13, 0
	global_atomic_add v163, v197, s[12:13]
	global_atomic_add v163, v197, s[12:13] offset:256
	global_atomic_add v163, v197, s[12:13] offset:512
	global_atomic_add v163, v197, s[12:13] offset:768
	global_atomic_add v163, v197, s[12:13] offset:1024
	global_atomic_add v163, v197, s[12:13] offset:1280
	global_atomic_add v163, v197, s[12:13] offset:1536
	global_atomic_add v163, v197, s[12:13] offset:1792
	global_atomic_add v163, v197, s[12:13] offset:2048
	global_atomic_add v163, v197, s[12:13] offset:2304
	global_atomic_add v163, v197, s[12:13] offset:2560
	global_atomic_add v163, v197, s[12:13] offset:2816
	global_atomic_add v163, v197, s[12:13] offset:3072
	global_atomic_add v163, v197, s[12:13] offset:3328
	global_atomic_add v163, v197, s[12:13] offset:3584
	global_atomic_add v163, v197, s[12:13] offset:3840
	s_mov_b32 s5, 0

; __device__ __forceinline__ unsigned xb_ld(unsigned* p)              { return __hip_atomic_load(p, __ATOMIC_RELAXED, __HIP_MEMORY_SCOPE_AGENT); }
; __device__ __forceinline__ unsigned xb_add(unsigned* p, unsigned v) { return __hip_atomic_fetch_add(p, v, __ATOMIC_RELAXED, __HIP_MEMORY_SCOPE_AGENT); }
; #define XB_SPIN(cond, bar) do { unsigned _sp = 0; while (cond) { __builtin_amdgcn_s_sleep(1); \
;     if ((++_sp & 255u) == 0u) { if (xb_ld(&(bar)[XB_TMO])) break; if (_sp > XB_SPIN_CAP) { atomicAdd(&(bar)[XB_TMO], 1u); break; } } } } while (0)
; __device__ __forceinline__ void xcd_barrier(const XcdBarrier& b) {
;     ...
;         if (old + 1u == (gen + 1u) * nloc) {
;             __builtin_amdgcn_fence(__ATOMIC_RELEASE, "agent");
;             asm volatile("s_waitcnt vmcnt(0)" ::: "memory");
;             const unsigned og = xb_add(&bar[XB_TOP], 1u);
;             const unsigned tg = og / nx;
;             if (og + 1u == (tg + 1u) * nx) xb_add(&bar[XB_TOPGEN], 1u);
;             else XB_SPIN(xb_ld(&bar[XB_TOPGEN]) == tg, bar);
;             __builtin_amdgcn_fence(__ATOMIC_ACQUIRE, "agent");
;             xb_add(&bar[XB_XGEN(b.x)], 1u);
;             asm volatile("s_waitcnt vmcnt(0)" ::: "memory");
;         } else {
;             XB_SPIN(xb_ld(&bar[XB_XGEN(b.x)]) == gen, bar);
;             __builtin_amdgcn_fence(__ATOMIC_ACQUIRE, "agent");
;             asm volatile("s_waitcnt vmcnt(0)" ::: "memory");
.Lbar_nl_done_11:
	s_waitcnt vmcnt(0)
.LBB0_392:
	s_andn2_saveexec_b64 s[6:7], s[6:7]
	s_cbranch_execz .LBB0_412
	s_mov_b64 s[6:7], exec
	buffer_wbl2 sc1
	s_waitcnt lgkmcnt(0)
	s_waitcnt vmcnt(0)
	v_readlane_b32 s18, v253, 48
	v_readlane_b32 s19, v253, 49
	v_readlane_b32 s12, v253, 52
	v_readlane_b32 s13, v253, 53
	s_nop 3
	s_add_u32 s18, s18, 0x3600
	s_addc_u32 s19, s19, 0
	s_add_u32 s12, s12, 0x2500
	s_addc_u32 s13, s13, 0
	global_atomic_add v163, v197, s[12:13]
	global_atomic_add v163, v197, s[12:13] offset:256
	global_atomic_add v163, v197, s[12:13] offset:512
	global_atomic_add v163, v197, s[12:13] offset:768
	global_atomic_add v163, v197, s[12:13] offset:1024
	global_atomic_add v163, v197, s[12:13] offset:1280
	global_atomic_add v163, v197, s[12:13] offset:1536
	global_atomic_add v163, v197, s[12:13] offset:1792
	global_atomic_add v163, v197, s[12:13] offset:2048
	global_atomic_add v163, v197, s[12:13] offset:2304
	global_atomic_add v163, v197, s[12:13] offset:2560
	global_atomic_add v163, v197, s[12:13] offset:2816
	global_atomic_add v163, v197, s[12:13] offset:3072
	global_atomic_add v163, v197, s[12:13] offset:3328
	global_atomic_add v163, v197, s[12:13] offset:3584
	global_atomic_add v163, v197, s[12:13] offset:3840
	s_mov_b32 s5, 0

; __device__ __forceinline__ unsigned xb_ld(unsigned* p)              { return __hip_atomic_load(p, __ATOMIC_RELAXED, __HIP_MEMORY_SCOPE_AGENT); }
; __device__ __forceinline__ unsigned xb_add(unsigned* p, unsigned v) { return __hip_atomic_fetch_add(p, v, __ATOMIC_RELAXED, __HIP_MEMORY_SCOPE_AGENT); }
; #define XB_SPIN(cond, bar) do { unsigned _sp = 0; while (cond) { __builtin_amdgcn_s_sleep(1); \
;     if ((++_sp & 255u) == 0u) { if (xb_ld(&(bar)[XB_TMO])) break; if (_sp > XB_SPIN_CAP) { atomicAdd(&(bar)[XB_TMO], 1u); break; } } } } while (0)
; __device__ __forceinline__ void xcd_barrier(const XcdBarrier& b) {
;     ...
;         if (old + 1u == (gen + 1u) * nloc) {
;             __builtin_amdgcn_fence(__ATOMIC_RELEASE, "agent");
;             asm volatile("s_waitcnt vmcnt(0)" ::: "memory");
;             const unsigned og = xb_add(&bar[XB_TOP], 1u);
;             const unsigned tg = og / nx;
;             if (og + 1u == (tg + 1u) * nx) xb_add(&bar[XB_TOPGEN], 1u);
;             else XB_SPIN(xb_ld(&bar[XB_TOPGEN]) == tg, bar);
;             __builtin_amdgcn_fence(__ATOMIC_ACQUIRE, "agent");
;             xb_add(&bar[XB_XGEN(b.x)], 1u);
;             asm volatile("s_waitcnt vmcnt(0)" ::: "memory");
;         } else {
;             XB_SPIN(xb_ld(&bar[XB_XGEN(b.x)]) == gen, bar);
;             __builtin_amdgcn_fence(__ATOMIC_ACQUIRE, "agent");
;             asm volatile("s_waitcnt vmcnt(0)" ::: "memory");
.Lbar_nl_done_10:
	s_waitcnt vmcnt(0)
.LBB0_507:
	s_andn2_saveexec_b64 s[6:7], s[6:7]
	s_cbranch_execz .LBB0_527
	s_mov_b64 s[6:7], exec
	buffer_wbl2 sc1
	s_waitcnt lgkmcnt(0)
	s_waitcnt vmcnt(0)
	v_readlane_b32 s18, v253, 48
	v_readlane_b32 s19, v253, 49
	v_readlane_b32 s12, v253, 52
	v_readlane_b32 s13, v253, 53
	s_nop 3
	s_add_u32 s18, s18, 0x3600
	s_addc_u32 s19, s19, 0
	s_add_u32 s12, s12, 0x2500
	s_addc_u32 s13, s13, 0
	global_atomic_add v163, v197, s[12:13]
	global_atomic_add v163, v197, s[12:13] offset:256
	global_atomic_add v163, v197, s[12:13] offset:512
	global_atomic_add v163, v197, s[12:13] offset:768
	global_atomic_add v163, v197, s[12:13] offset:1024
	global_atomic_add v163, v197, s[12:13] offset:1280
	global_atomic_add v163, v197, s[12:13] offset:1536
	global_atomic_add v163, v197, s[12:13] offset:1792
	global_atomic_add v163, v197, s[12:13] offset:2048
	global_atomic_add v163, v197, s[12:13] offset:2304
	global_atomic_add v163, v197, s[12:13] offset:2560
	global_atomic_add v163, v197, s[12:13] offset:2816
	global_atomic_add v163, v197, s[12:13] offset:3072
	global_atomic_add v163, v197, s[12:13] offset:3328
	global_atomic_add v163, v197, s[12:13] offset:3584
	global_atomic_add v163, v197, s[12:13] offset:3840
	s_mov_b32 s5, 0

; __device__ __forceinline__ unsigned xb_ld(unsigned* p)              { return __hip_atomic_load(p, __ATOMIC_RELAXED, __HIP_MEMORY_SCOPE_AGENT); }
; __device__ __forceinline__ unsigned xb_add(unsigned* p, unsigned v) { return __hip_atomic_fetch_add(p, v, __ATOMIC_RELAXED, __HIP_MEMORY_SCOPE_AGENT); }
; #define XB_SPIN(cond, bar) do { unsigned _sp = 0; while (cond) { __builtin_amdgcn_s_sleep(1); \
;     if ((++_sp & 255u) == 0u) { if (xb_ld(&(bar)[XB_TMO])) break; if (_sp > XB_SPIN_CAP) { atomicAdd(&(bar)[XB_TMO], 1u); break; } } } } while (0)
; __device__ __forceinline__ void xcd_barrier(const XcdBarrier& b) {
;     ...
;         if (old + 1u == (gen + 1u) * nloc) {
;             __builtin_amdgcn_fence(__ATOMIC_RELEASE, "agent");
;             asm volatile("s_waitcnt vmcnt(0)" ::: "memory");
;             const unsigned og = xb_add(&bar[XB_TOP], 1u);
;             const unsigned tg = og / nx;
;             if (og + 1u == (tg + 1u) * nx) xb_add(&bar[XB_TOPGEN], 1u);
;             else XB_SPIN(xb_ld(&bar[XB_TOPGEN]) == tg, bar);
;             __builtin_amdgcn_fence(__ATOMIC_ACQUIRE, "agent");
;             xb_add(&bar[XB_XGEN(b.x)], 1u);
;             asm volatile("s_waitcnt vmcnt(0)" ::: "memory");
;         } else {
;             XB_SPIN(xb_ld(&bar[XB_XGEN(b.x)]) == gen, bar);
;             __builtin_amdgcn_fence(__ATOMIC_ACQUIRE, "agent");
;             asm volatile("s_waitcnt vmcnt(0)" ::: "memory");
.Lbar_nl_done_9:
	s_waitcnt vmcnt(0)
.LBB0_736:
	s_andn2_saveexec_b64 s[6:7], s[6:7]
	s_cbranch_execz .LBB0_756
	s_mov_b64 s[6:7], exec
	buffer_wbl2 sc1
	s_waitcnt lgkmcnt(0)
	s_waitcnt vmcnt(0)
	v_readlane_b32 s18, v253, 48
	v_readlane_b32 s19, v253, 49
	v_readlane_b32 s12, v253, 52
	v_readlane_b32 s13, v253, 53
	s_nop 3
	s_add_u32 s18, s18, 0x3600
	s_addc_u32 s19, s19, 0
	s_add_u32 s12, s12, 0x2500
	s_addc_u32 s13, s13, 0
	global_atomic_add v163, v197, s[12:13]
	global_atomic_add v163, v197, s[12:13] offset:256
	global_atomic_add v163, v197, s[12:13] offset:512
	global_atomic_add v163, v197, s[12:13] offset:768
	global_atomic_add v163, v197, s[12:13] offset:1024
	global_atomic_add v163, v197, s[12:13] offset:1280
	global_atomic_add v163, v197, s[12:13] offset:1536
	global_atomic_add v163, v197, s[12:13] offset:1792
	global_atomic_add v163, v197, s[12:13] offset:2048
	global_atomic_add v163, v197, s[12:13] offset:2304
	global_atomic_add v163, v197, s[12:13] offset:2560
	global_atomic_add v163, v197, s[12:13] offset:2816
	global_atomic_add v163, v197, s[12:13] offset:3072
	global_atomic_add v163, v197, s[12:13] offset:3328
	global_atomic_add v163, v197, s[12:13] offset:3584
	global_atomic_add v163, v197, s[12:13] offset:3840
	s_mov_b32 s5, 0

; __device__ __forceinline__ unsigned xb_ld(unsigned* p)              { return __hip_atomic_load(p, __ATOMIC_RELAXED, __HIP_MEMORY_SCOPE_AGENT); }
; __device__ __forceinline__ unsigned xb_add(unsigned* p, unsigned v) { return __hip_atomic_fetch_add(p, v, __ATOMIC_RELAXED, __HIP_MEMORY_SCOPE_AGENT); }
; #define XB_SPIN(cond, bar) do { unsigned _sp = 0; while (cond) { __builtin_amdgcn_s_sleep(1); \
;     if ((++_sp & 255u) == 0u) { if (xb_ld(&(bar)[XB_TMO])) break; if (_sp > XB_SPIN_CAP) { atomicAdd(&(bar)[XB_TMO], 1u); break; } } } } while (0)
; __device__ __forceinline__ void xcd_barrier(const XcdBarrier& b) {
;     ...
;         if (old + 1u == (gen + 1u) * nloc) {
;             __builtin_amdgcn_fence(__ATOMIC_RELEASE, "agent");
;             asm volatile("s_waitcnt vmcnt(0)" ::: "memory");
;             const unsigned og = xb_add(&bar[XB_TOP], 1u);
;             const unsigned tg = og / nx;
;             if (og + 1u == (tg + 1u) * nx) xb_add(&bar[XB_TOPGEN], 1u);
;             else XB_SPIN(xb_ld(&bar[XB_TOPGEN]) == tg, bar);
;             __builtin_amdgcn_fence(__ATOMIC_ACQUIRE, "agent");
;             xb_add(&bar[XB_XGEN(b.x)], 1u);
;             asm volatile("s_waitcnt vmcnt(0)" ::: "memory");
;         } else {
;             XB_SPIN(xb_ld(&bar[XB_XGEN(b.x)]) == gen, bar);
;             __builtin_amdgcn_fence(__ATOMIC_ACQUIRE, "agent");
;             asm volatile("s_waitcnt vmcnt(0)" ::: "memory");
.Lbar_nl_done_8:
	s_waitcnt vmcnt(0)
.LBB0_833:
	s_andn2_saveexec_b64 s[6:7], s[6:7]
	s_cbranch_execz .LBB0_853
	s_mov_b64 s[6:7], exec
	buffer_wbl2 sc1
	s_waitcnt lgkmcnt(0)
	s_waitcnt vmcnt(0)
	v_readlane_b32 s18, v253, 48
	v_readlane_b32 s19, v253, 49
	v_readlane_b32 s12, v253, 52
	v_readlane_b32 s13, v253, 53
	s_nop 3
	s_add_u32 s18, s18, 0x3600
	s_addc_u32 s19, s19, 0
	s_add_u32 s12, s12, 0x2500
	s_addc_u32 s13, s13, 0
	global_atomic_add v163, v197, s[12:13]
	global_atomic_add v163, v197, s[12:13] offset:256
	global_atomic_add v163, v197, s[12:13] offset:512
	global_atomic_add v163, v197, s[12:13] offset:768
	global_atomic_add v163, v197, s[12:13] offset:1024
	global_atomic_add v163, v197, s[12:13] offset:1280
	global_atomic_add v163, v197, s[12:13] offset:1536
	global_atomic_add v163, v197, s[12:13] offset:1792
	global_atomic_add v163, v197, s[12:13] offset:2048
	global_atomic_add v163, v197, s[12:13] offset:2304
	global_atomic_add v163, v197, s[12:13] offset:2560
	global_atomic_add v163, v197, s[12:13] offset:2816
	global_atomic_add v163, v197, s[12:13] offset:3072
	global_atomic_add v163, v197, s[12:13] offset:3328
	global_atomic_add v163, v197, s[12:13] offset:3584
	global_atomic_add v163, v197, s[12:13] offset:3840
	s_mov_b32 s5, 0

; __device__ __forceinline__ unsigned xb_ld(unsigned* p)              { return __hip_atomic_load(p, __ATOMIC_RELAXED, __HIP_MEMORY_SCOPE_AGENT); }
; __device__ __forceinline__ unsigned xb_add(unsigned* p, unsigned v) { return __hip_atomic_fetch_add(p, v, __ATOMIC_RELAXED, __HIP_MEMORY_SCOPE_AGENT); }
; #define XB_SPIN(cond, bar) do { unsigned _sp = 0; while (cond) { __builtin_amdgcn_s_sleep(1); \
;     if ((++_sp & 255u) == 0u) { if (xb_ld(&(bar)[XB_TMO])) break; if (_sp > XB_SPIN_CAP) { atomicAdd(&(bar)[XB_TMO], 1u); break; } } } } while (0)
; __device__ __forceinline__ void xcd_barrier(const XcdBarrier& b) {
;     ...
;         if (old + 1u == (gen + 1u) * nloc) {
;             __builtin_amdgcn_fence(__ATOMIC_RELEASE, "agent");
;             asm volatile("s_waitcnt vmcnt(0)" ::: "memory");
;             const unsigned og = xb_add(&bar[XB_TOP], 1u);
;             const unsigned tg = og / nx;
;             if (og + 1u == (tg + 1u) * nx) xb_add(&bar[XB_TOPGEN], 1u);
;             else XB_SPIN(xb_ld(&bar[XB_TOPGEN]) == tg, bar);
;             __builtin_amdgcn_fence(__ATOMIC_ACQUIRE, "agent");
;             xb_add(&bar[XB_XGEN(b.x)], 1u);
;             asm volatile("s_waitcnt vmcnt(0)" ::: "memory");
;         } else {
;             XB_SPIN(xb_ld(&bar[XB_XGEN(b.x)]) == gen, bar);
;             __builtin_amdgcn_fence(__ATOMIC_ACQUIRE, "agent");
;             asm volatile("s_waitcnt vmcnt(0)" ::: "memory");
.Lbar_nl_done_7:
	s_waitcnt vmcnt(0)
.LBB0_959:
	s_andn2_saveexec_b64 s[6:7], s[6:7]
	s_cbranch_execz .LBB0_979
	s_mov_b64 s[6:7], exec
	buffer_wbl2 sc1
	s_waitcnt lgkmcnt(0)
	s_waitcnt vmcnt(0)
	v_readlane_b32 s18, v253, 48
	v_readlane_b32 s19, v253, 49
	v_readlane_b32 s12, v253, 52
	v_readlane_b32 s13, v253, 53
	s_nop 3
	s_add_u32 s18, s18, 0x3600
	s_addc_u32 s19, s19, 0
	s_add_u32 s12, s12, 0x2500
	s_addc_u32 s13, s13, 0
	global_atomic_add v163, v197, s[12:13]
	global_atomic_add v163, v197, s[12:13] offset:256
	global_atomic_add v163, v197, s[12:13] offset:512
	global_atomic_add v163, v197, s[12:13] offset:768
	global_atomic_add v163, v197, s[12:13] offset:1024
	global_atomic_add v163, v197, s[12:13] offset:1280
	global_atomic_add v163, v197, s[12:13] offset:1536
	global_atomic_add v163, v197, s[12:13] offset:1792
	global_atomic_add v163, v197, s[12:13] offset:2048
	global_atomic_add v163, v197, s[12:13] offset:2304
	global_atomic_add v163, v197, s[12:13] offset:2560
	global_atomic_add v163, v197, s[12:13] offset:2816
	global_atomic_add v163, v197, s[12:13] offset:3072
	global_atomic_add v163, v197, s[12:13] offset:3328
	global_atomic_add v163, v197, s[12:13] offset:3584
	global_atomic_add v163, v197, s[12:13] offset:3840
	s_mov_b32 s5, 0

; __device__ __forceinline__ unsigned xb_ld(unsigned* p)              { return __hip_atomic_load(p, __ATOMIC_RELAXED, __HIP_MEMORY_SCOPE_AGENT); }
; __device__ __forceinline__ unsigned xb_add(unsigned* p, unsigned v) { return __hip_atomic_fetch_add(p, v, __ATOMIC_RELAXED, __HIP_MEMORY_SCOPE_AGENT); }
; #define XB_SPIN(cond, bar) do { unsigned _sp = 0; while (cond) { __builtin_amdgcn_s_sleep(1); \
;     if ((++_sp & 255u) == 0u) { if (xb_ld(&(bar)[XB_TMO])) break; if (_sp > XB_SPIN_CAP) { atomicAdd(&(bar)[XB_TMO], 1u); break; } } } } while (0)
; __device__ __forceinline__ void xcd_barrier(const XcdBarrier& b) {
;     ...
;         if (old + 1u == (gen + 1u) * nloc) {
;             __builtin_amdgcn_fence(__ATOMIC_RELEASE, "agent");
;             asm volatile("s_waitcnt vmcnt(0)" ::: "memory");
;             const unsigned og = xb_add(&bar[XB_TOP], 1u);
;             const unsigned tg = og / nx;
;             if (og + 1u == (tg + 1u) * nx) xb_add(&bar[XB_TOPGEN], 1u);
;             else XB_SPIN(xb_ld(&bar[XB_TOPGEN]) == tg, bar);
;             __builtin_amdgcn_fence(__ATOMIC_ACQUIRE, "agent");
;             xb_add(&bar[XB_XGEN(b.x)], 1u);
;             asm volatile("s_waitcnt vmcnt(0)" ::: "memory");
;         } else {
;             XB_SPIN(xb_ld(&bar[XB_XGEN(b.x)]) == gen, bar);
;             __builtin_amdgcn_fence(__ATOMIC_ACQUIRE, "agent");
;             asm volatile("s_waitcnt vmcnt(0)" ::: "memory");
.Lbar_nl_done_6:
	s_waitcnt vmcnt(0)
.LBB0_1019:
	s_andn2_saveexec_b64 s[6:7], s[6:7]
	s_cbranch_execz .LBB0_1039
	s_mov_b64 s[6:7], exec
	buffer_wbl2 sc1
	s_waitcnt lgkmcnt(0)
	s_waitcnt vmcnt(0)
	v_readlane_b32 s18, v253, 48
	v_readlane_b32 s19, v253, 49
	v_readlane_b32 s12, v253, 52
	v_readlane_b32 s13, v253, 53
	s_nop 3
	s_add_u32 s18, s18, 0x3600
	s_addc_u32 s19, s19, 0
	s_add_u32 s12, s12, 0x2500
	s_addc_u32 s13, s13, 0
	global_atomic_add v163, v197, s[12:13]
	global_atomic_add v163, v197, s[12:13] offset:256
	global_atomic_add v163, v197, s[12:13] offset:512
	global_atomic_add v163, v197, s[12:13] offset:768
	global_atomic_add v163, v197, s[12:13] offset:1024
	global_atomic_add v163, v197, s[12:13] offset:1280
	global_atomic_add v163, v197, s[12:13] offset:1536
	global_atomic_add v163, v197, s[12:13] offset:1792
	global_atomic_add v163, v197, s[12:13] offset:2048
	global_atomic_add v163, v197, s[12:13] offset:2304
	global_atomic_add v163, v197, s[12:13] offset:2560
	global_atomic_add v163, v197, s[12:13] offset:2816
	global_atomic_add v163, v197, s[12:13] offset:3072
	global_atomic_add v163, v197, s[12:13] offset:3328
	global_atomic_add v163, v197, s[12:13] offset:3584
	global_atomic_add v163, v197, s[12:13] offset:3840
	s_mov_b32 s5, 0

; __device__ __forceinline__ unsigned xb_ld(unsigned* p)              { return __hip_atomic_load(p, __ATOMIC_RELAXED, __HIP_MEMORY_SCOPE_AGENT); }
; __device__ __forceinline__ unsigned xb_add(unsigned* p, unsigned v) { return __hip_atomic_fetch_add(p, v, __ATOMIC_RELAXED, __HIP_MEMORY_SCOPE_AGENT); }
; #define XB_SPIN(cond, bar) do { unsigned _sp = 0; while (cond) { __builtin_amdgcn_s_sleep(1); \
;     if ((++_sp & 255u) == 0u) { if (xb_ld(&(bar)[XB_TMO])) break; if (_sp > XB_SPIN_CAP) { atomicAdd(&(bar)[XB_TMO], 1u); break; } } } } while (0)
; __device__ __forceinline__ void xcd_barrier(const XcdBarrier& b) {
;     ...
;         if (old + 1u == (gen + 1u) * nloc) {
;             __builtin_amdgcn_fence(__ATOMIC_RELEASE, "agent");
;             asm volatile("s_waitcnt vmcnt(0)" ::: "memory");
;             const unsigned og = xb_add(&bar[XB_TOP], 1u);
;             const unsigned tg = og / nx;
;             if (og + 1u == (tg + 1u) * nx) xb_add(&bar[XB_TOPGEN], 1u);
;             else XB_SPIN(xb_ld(&bar[XB_TOPGEN]) == tg, bar);
;             __builtin_amdgcn_fence(__ATOMIC_ACQUIRE, "agent");
;             xb_add(&bar[XB_XGEN(b.x)], 1u);
;             asm volatile("s_waitcnt vmcnt(0)" ::: "memory");
;         } else {
;             XB_SPIN(xb_ld(&bar[XB_XGEN(b.x)]) == gen, bar);
;             __builtin_amdgcn_fence(__ATOMIC_ACQUIRE, "agent");
;             asm volatile("s_waitcnt vmcnt(0)" ::: "memory");
.Lbar_nl_done_5:
	s_waitcnt vmcnt(0)
.LBB0_1096:
	s_andn2_saveexec_b64 s[6:7], s[6:7]
	s_cbranch_execz .LBB0_1116
	s_mov_b64 s[6:7], exec
	buffer_wbl2 sc1
	s_waitcnt lgkmcnt(0)
	s_waitcnt vmcnt(0)
	v_readlane_b32 s18, v253, 48
	v_readlane_b32 s19, v253, 49
	v_readlane_b32 s12, v253, 52
	v_readlane_b32 s13, v253, 53
	s_nop 3
	s_add_u32 s18, s18, 0x3600
	s_addc_u32 s19, s19, 0
	s_add_u32 s12, s12, 0x2500
	s_addc_u32 s13, s13, 0
	global_atomic_add v163, v197, s[12:13]
	global_atomic_add v163, v197, s[12:13] offset:256
	global_atomic_add v163, v197, s[12:13] offset:512
	global_atomic_add v163, v197, s[12:13] offset:768
	global_atomic_add v163, v197, s[12:13] offset:1024
	global_atomic_add v163, v197, s[12:13] offset:1280
	global_atomic_add v163, v197, s[12:13] offset:1536
	global_atomic_add v163, v197, s[12:13] offset:1792
	global_atomic_add v163, v197, s[12:13] offset:2048
	global_atomic_add v163, v197, s[12:13] offset:2304
	global_atomic_add v163, v197, s[12:13] offset:2560
	global_atomic_add v163, v197, s[12:13] offset:2816
	global_atomic_add v163, v197, s[12:13] offset:3072
	global_atomic_add v163, v197, s[12:13] offset:3328
	global_atomic_add v163, v197, s[12:13] offset:3584
	global_atomic_add v163, v197, s[12:13] offset:3840
	s_mov_b32 s5, 0

; __device__ __forceinline__ unsigned xb_ld(unsigned* p)              { return __hip_atomic_load(p, __ATOMIC_RELAXED, __HIP_MEMORY_SCOPE_AGENT); }
; __device__ __forceinline__ unsigned xb_add(unsigned* p, unsigned v) { return __hip_atomic_fetch_add(p, v, __ATOMIC_RELAXED, __HIP_MEMORY_SCOPE_AGENT); }
; #define XB_SPIN(cond, bar) do { unsigned _sp = 0; while (cond) { __builtin_amdgcn_s_sleep(1); \
;     if ((++_sp & 255u) == 0u) { if (xb_ld(&(bar)[XB_TMO])) break; if (_sp > XB_SPIN_CAP) { atomicAdd(&(bar)[XB_TMO], 1u); break; } } } } while (0)
; __device__ __forceinline__ void xcd_barrier(const XcdBarrier& b) {
;     ...
;         if (old + 1u == (gen + 1u) * nloc) {
;             __builtin_amdgcn_fence(__ATOMIC_RELEASE, "agent");
;             asm volatile("s_waitcnt vmcnt(0)" ::: "memory");
;             const unsigned og = xb_add(&bar[XB_TOP], 1u);
;             const unsigned tg = og / nx;
;             if (og + 1u == (tg + 1u) * nx) xb_add(&bar[XB_TOPGEN], 1u);
;             else XB_SPIN(xb_ld(&bar[XB_TOPGEN]) == tg, bar);
;             __builtin_amdgcn_fence(__ATOMIC_ACQUIRE, "agent");
;             xb_add(&bar[XB_XGEN(b.x)], 1u);
;             asm volatile("s_waitcnt vmcnt(0)" ::: "memory");
;         } else {
;             XB_SPIN(xb_ld(&bar[XB_XGEN(b.x)]) == gen, bar);
;             __builtin_amdgcn_fence(__ATOMIC_ACQUIRE, "agent");
;             asm volatile("s_waitcnt vmcnt(0)" ::: "memory");
.Lbar_nl_done_4:
	s_waitcnt vmcnt(0)
.LBB0_1172:
	s_andn2_saveexec_b64 s[6:7], s[6:7]
	s_cbranch_execz .LBB0_1192
	s_mov_b64 s[6:7], exec
	buffer_wbl2 sc1
	s_waitcnt lgkmcnt(0)
	s_waitcnt vmcnt(0)
	v_readlane_b32 s18, v253, 48
	v_readlane_b32 s19, v253, 49
	v_readlane_b32 s12, v253, 52
	v_readlane_b32 s13, v253, 53
	s_nop 3
	s_add_u32 s18, s18, 0x3600
	s_addc_u32 s19, s19, 0
	s_add_u32 s12, s12, 0x2500
	s_addc_u32 s13, s13, 0
	global_atomic_add v163, v197, s[12:13]
	global_atomic_add v163, v197, s[12:13] offset:256
	global_atomic_add v163, v197, s[12:13] offset:512
	global_atomic_add v163, v197, s[12:13] offset:768
	global_atomic_add v163, v197, s[12:13] offset:1024
	global_atomic_add v163, v197, s[12:13] offset:1280
	global_atomic_add v163, v197, s[12:13] offset:1536
	global_atomic_add v163, v197, s[12:13] offset:1792
	global_atomic_add v163, v197, s[12:13] offset:2048
	global_atomic_add v163, v197, s[12:13] offset:2304
	global_atomic_add v163, v197, s[12:13] offset:2560
	global_atomic_add v163, v197, s[12:13] offset:2816
	global_atomic_add v163, v197, s[12:13] offset:3072
	global_atomic_add v163, v197, s[12:13] offset:3328
	global_atomic_add v163, v197, s[12:13] offset:3584
	global_atomic_add v163, v197, s[12:13] offset:3840
	s_mov_b32 s5, 0

; __device__ __forceinline__ unsigned xb_ld(unsigned* p)              { return __hip_atomic_load(p, __ATOMIC_RELAXED, __HIP_MEMORY_SCOPE_AGENT); }
; __device__ __forceinline__ unsigned xb_add(unsigned* p, unsigned v) { return __hip_atomic_fetch_add(p, v, __ATOMIC_RELAXED, __HIP_MEMORY_SCOPE_AGENT); }
; #define XB_SPIN(cond, bar) do { unsigned _sp = 0; while (cond) { __builtin_amdgcn_s_sleep(1); \
;     if ((++_sp & 255u) == 0u) { if (xb_ld(&(bar)[XB_TMO])) break; if (_sp > XB_SPIN_CAP) { atomicAdd(&(bar)[XB_TMO], 1u); break; } } } } while (0)
; __device__ __forceinline__ void xcd_barrier(const XcdBarrier& b) {
;     ...
;         if (old + 1u == (gen + 1u) * nloc) {
;             __builtin_amdgcn_fence(__ATOMIC_RELEASE, "agent");
;             asm volatile("s_waitcnt vmcnt(0)" ::: "memory");
;             const unsigned og = xb_add(&bar[XB_TOP], 1u);
;             const unsigned tg = og / nx;
;             if (og + 1u == (tg + 1u) * nx) xb_add(&bar[XB_TOPGEN], 1u);
;             else XB_SPIN(xb_ld(&bar[XB_TOPGEN]) == tg, bar);
;             __builtin_amdgcn_fence(__ATOMIC_ACQUIRE, "agent");
;             xb_add(&bar[XB_XGEN(b.x)], 1u);
;             asm volatile("s_waitcnt vmcnt(0)" ::: "memory");
;         } else {
;             XB_SPIN(xb_ld(&bar[XB_XGEN(b.x)]) == gen, bar);
;             __builtin_amdgcn_fence(__ATOMIC_ACQUIRE, "agent");
;             asm volatile("s_waitcnt vmcnt(0)" ::: "memory");
.Lbar_nl_done_3:
	s_waitcnt vmcnt(0)
.LBB0_1294:
	s_andn2_saveexec_b64 s[6:7], s[6:7]
	s_cbranch_execz .LBB0_1314
	s_mov_b64 s[6:7], exec
	buffer_wbl2 sc1
	s_waitcnt lgkmcnt(0)
	s_waitcnt vmcnt(0)
	v_readlane_b32 s18, v253, 48
	v_readlane_b32 s19, v253, 49
	v_readlane_b32 s12, v253, 52
	v_readlane_b32 s13, v253, 53
	s_nop 3
	s_add_u32 s18, s18, 0x3600
	s_addc_u32 s19, s19, 0
	s_add_u32 s12, s12, 0x2500
	s_addc_u32 s13, s13, 0
	global_atomic_add v163, v197, s[12:13]
	global_atomic_add v163, v197, s[12:13] offset:256
	global_atomic_add v163, v197, s[12:13] offset:512
	global_atomic_add v163, v197, s[12:13] offset:768
	global_atomic_add v163, v197, s[12:13] offset:1024
	global_atomic_add v163, v197, s[12:13] offset:1280
	global_atomic_add v163, v197, s[12:13] offset:1536
	global_atomic_add v163, v197, s[12:13] offset:1792
	global_atomic_add v163, v197, s[12:13] offset:2048
	global_atomic_add v163, v197, s[12:13] offset:2304
	global_atomic_add v163, v197, s[12:13] offset:2560
	global_atomic_add v163, v197, s[12:13] offset:2816
	global_atomic_add v163, v197, s[12:13] offset:3072
	global_atomic_add v163, v197, s[12:13] offset:3328
	global_atomic_add v163, v197, s[12:13] offset:3584
	global_atomic_add v163, v197, s[12:13] offset:3840
	s_mov_b32 s5, 0

; __device__ __forceinline__ unsigned xb_ld(unsigned* p)              { return __hip_atomic_load(p, __ATOMIC_RELAXED, __HIP_MEMORY_SCOPE_AGENT); }
; __device__ __forceinline__ unsigned xb_add(unsigned* p, unsigned v) { return __hip_atomic_fetch_add(p, v, __ATOMIC_RELAXED, __HIP_MEMORY_SCOPE_AGENT); }
; #define XB_SPIN(cond, bar) do { unsigned _sp = 0; while (cond) { __builtin_amdgcn_s_sleep(1); \
;     if ((++_sp & 255u) == 0u) { if (xb_ld(&(bar)[XB_TMO])) break; if (_sp > XB_SPIN_CAP) { atomicAdd(&(bar)[XB_TMO], 1u); break; } } } } while (0)
; __device__ __forceinline__ void xcd_barrier(const XcdBarrier& b) {
;     ...
;         if (old + 1u == (gen + 1u) * nloc) {
;             __builtin_amdgcn_fence(__ATOMIC_RELEASE, "agent");
;             asm volatile("s_waitcnt vmcnt(0)" ::: "memory");
;             const unsigned og = xb_add(&bar[XB_TOP], 1u);
;             const unsigned tg = og / nx;
;             if (og + 1u == (tg + 1u) * nx) xb_add(&bar[XB_TOPGEN], 1u);
;             else XB_SPIN(xb_ld(&bar[XB_TOPGEN]) == tg, bar);
;             __builtin_amdgcn_fence(__ATOMIC_ACQUIRE, "agent");
;             xb_add(&bar[XB_XGEN(b.x)], 1u);
;             asm volatile("s_waitcnt vmcnt(0)" ::: "memory");
;         } else {
;             XB_SPIN(xb_ld(&bar[XB_XGEN(b.x)]) == gen, bar);
;             __builtin_amdgcn_fence(__ATOMIC_ACQUIRE, "agent");
;             asm volatile("s_waitcnt vmcnt(0)" ::: "memory");
.Lbar_nl_done_2:
	s_waitcnt vmcnt(0)
.LBB0_1415:
	s_andn2_saveexec_b64 s[6:7], s[6:7]
	s_cbranch_execz .LBB0_1435
	s_mov_b64 s[6:7], exec
	buffer_wbl2 sc1
	s_waitcnt lgkmcnt(0)
	s_waitcnt vmcnt(0)
	v_readlane_b32 s18, v253, 48
	v_readlane_b32 s19, v253, 49
	v_readlane_b32 s12, v253, 52
	v_readlane_b32 s13, v253, 53
	s_nop 3
	s_add_u32 s18, s18, 0x3600
	s_addc_u32 s19, s19, 0
	s_add_u32 s12, s12, 0x2500
	s_addc_u32 s13, s13, 0
	global_atomic_add v163, v197, s[12:13]
	global_atomic_add v163, v197, s[12:13] offset:256
	global_atomic_add v163, v197, s[12:13] offset:512
	global_atomic_add v163, v197, s[12:13] offset:768
	global_atomic_add v163, v197, s[12:13] offset:1024
	global_atomic_add v163, v197, s[12:13] offset:1280
	global_atomic_add v163, v197, s[12:13] offset:1536
	global_atomic_add v163, v197, s[12:13] offset:1792
	global_atomic_add v163, v197, s[12:13] offset:2048
	global_atomic_add v163, v197, s[12:13] offset:2304
	global_atomic_add v163, v197, s[12:13] offset:2560
	global_atomic_add v163, v197, s[12:13] offset:2816
	global_atomic_add v163, v197, s[12:13] offset:3072
	global_atomic_add v163, v197, s[12:13] offset:3328
	global_atomic_add v163, v197, s[12:13] offset:3584
	global_atomic_add v163, v197, s[12:13] offset:3840
	s_mov_b32 s5, 0

; __device__ __forceinline__ unsigned xb_ld(unsigned* p)              { return __hip_atomic_load(p, __ATOMIC_RELAXED, __HIP_MEMORY_SCOPE_AGENT); }
; __device__ __forceinline__ unsigned xb_add(unsigned* p, unsigned v) { return __hip_atomic_fetch_add(p, v, __ATOMIC_RELAXED, __HIP_MEMORY_SCOPE_AGENT); }
; #define XB_SPIN(cond, bar) do { unsigned _sp = 0; while (cond) { __builtin_amdgcn_s_sleep(1); \
;     if ((++_sp & 255u) == 0u) { if (xb_ld(&(bar)[XB_TMO])) break; if (_sp > XB_SPIN_CAP) { atomicAdd(&(bar)[XB_TMO], 1u); break; } } } } while (0)
; __device__ __forceinline__ void xcd_barrier(const XcdBarrier& b) {
;     ...
;         if (old + 1u == (gen + 1u) * nloc) {
;             __builtin_amdgcn_fence(__ATOMIC_RELEASE, "agent");
;             asm volatile("s_waitcnt vmcnt(0)" ::: "memory");
;             const unsigned og = xb_add(&bar[XB_TOP], 1u);
;             const unsigned tg = og / nx;
;             if (og + 1u == (tg + 1u) * nx) xb_add(&bar[XB_TOPGEN], 1u);
;             else XB_SPIN(xb_ld(&bar[XB_TOPGEN]) == tg, bar);
;             __builtin_amdgcn_fence(__ATOMIC_ACQUIRE, "agent");
;             xb_add(&bar[XB_XGEN(b.x)], 1u);
;             asm volatile("s_waitcnt vmcnt(0)" ::: "memory");
;         } else {
;             XB_SPIN(xb_ld(&bar[XB_XGEN(b.x)]) == gen, bar);
;             __builtin_amdgcn_fence(__ATOMIC_ACQUIRE, "agent");
;             asm volatile("s_waitcnt vmcnt(0)" ::: "memory");
.Lbar_nl_done_1:
	s_waitcnt vmcnt(0)
.LBB0_1477:
	s_andn2_saveexec_b64 s[6:7], s[6:7]
	s_cbranch_execz .LBB0_1497
	s_mov_b64 s[6:7], exec
	buffer_wbl2 sc1
	s_waitcnt lgkmcnt(0)
	s_waitcnt vmcnt(0)
	v_readlane_b32 s18, v253, 48
	v_readlane_b32 s19, v253, 49
	v_readlane_b32 s12, v253, 52
	v_readlane_b32 s13, v253, 53
	s_nop 3
	s_add_u32 s18, s18, 0x3600
	s_addc_u32 s19, s19, 0
	s_add_u32 s12, s12, 0x2500
	s_addc_u32 s13, s13, 0
	global_atomic_add v163, v197, s[12:13]
	global_atomic_add v163, v197, s[12:13] offset:256
	global_atomic_add v163, v197, s[12:13] offset:512
	global_atomic_add v163, v197, s[12:13] offset:768
	global_atomic_add v163, v197, s[12:13] offset:1024
	global_atomic_add v163, v197, s[12:13] offset:1280
	global_atomic_add v163, v197, s[12:13] offset:1536
	global_atomic_add v163, v197, s[12:13] offset:1792
	global_atomic_add v163, v197, s[12:13] offset:2048
	global_atomic_add v163, v197, s[12:13] offset:2304
	global_atomic_add v163, v197, s[12:13] offset:2560
	global_atomic_add v163, v197, s[12:13] offset:2816
	global_atomic_add v163, v197, s[12:13] offset:3072
	global_atomic_add v163, v197, s[12:13] offset:3328
	global_atomic_add v163, v197, s[12:13] offset:3584
	global_atomic_add v163, v197, s[12:13] offset:3840
	s_mov_b32 s5, 0

; __device__ __forceinline__ unsigned xb_ld(unsigned* p)              { return __hip_atomic_load(p, __ATOMIC_RELAXED, __HIP_MEMORY_SCOPE_AGENT); }
; __device__ __forceinline__ unsigned xb_add(unsigned* p, unsigned v) { return __hip_atomic_fetch_add(p, v, __ATOMIC_RELAXED, __HIP_MEMORY_SCOPE_AGENT); }
; #define XB_SPIN(cond, bar) do { unsigned _sp = 0; while (cond) { __builtin_amdgcn_s_sleep(1); \
;     if ((++_sp & 255u) == 0u) { if (xb_ld(&(bar)[XB_TMO])) break; if (_sp > XB_SPIN_CAP) { atomicAdd(&(bar)[XB_TMO], 1u); break; } } } } while (0)
; __device__ __forceinline__ void xcd_barrier(const XcdBarrier& b) {
;     ...
;         const unsigned old = xb_add(&bar[XB_XSUB(b.x)], 1u);
;         const unsigned gen = old / nloc;
;         if (old + 1u == (gen + 1u) * nloc) {
;             __builtin_amdgcn_fence(__ATOMIC_RELEASE, "agent");
;             asm volatile("s_waitcnt vmcnt(0)" ::: "memory");
;             const unsigned og = xb_add(&bar[XB_TOP], 1u);
;             const unsigned tg = og / nx;
;             if (og + 1u == (tg + 1u) * nx) xb_add(&bar[XB_TOPGEN], 1u);
;             else XB_SPIN(xb_ld(&bar[XB_TOPGEN]) == tg, bar);
;             __builtin_amdgcn_fence(__ATOMIC_ACQUIRE, "agent");
;             xb_add(&bar[XB_XGEN(b.x)], 1u);
;             asm volatile("s_waitcnt vmcnt(0)" ::: "memory");
;         } else {
;             XB_SPIN(xb_ld(&bar[XB_XGEN(b.x)]) == gen, bar);
.LBB0_1538:
	s_or_b64 exec, exec, s[6:7]
	v_cvt_f32_u32_e32 v5, v3
	s_waitcnt vmcnt(0)
	buffer_inv sc1
	v_readfirstlane_b32 s4, v4
	v_sub_u32_e32 v4, 0, v3
	v_rcp_iflag_f32_e32 v5, v5
	v_add_u32_e32 v6, s4, v1
	v_mul_f32_e32 v5, 0x4f7ffffe, v5
	v_cvt_u32_f32_e32 v5, v5
	v_mul_lo_u32 v1, v4, v5
	v_mul_hi_u32 v1, v5, v1
	v_add_u32_e32 v1, v5, v1
	v_mul_hi_u32 v1, v6, v1
	v_mul_lo_u32 v4, v1, v3
	v_sub_u32_e32 v4, v6, v4
	v_add_u32_e32 v5, 1, v1
	v_cmp_ge_u32_e32 vcc, v4, v3
	s_nop 1
	v_cndmask_b32_e32 v1, v1, v5, vcc
	v_sub_u32_e32 v5, v4, v3
	v_cndmask_b32_e32 v4, v4, v5, vcc
	v_add_u32_e32 v5, 1, v1
	v_cmp_ge_u32_e32 vcc, v4, v3
	v_add_u32_e32 v4, 1, v6
	s_nop 0
	v_cndmask_b32_e32 v1, v1, v5, vcc
	v_mul_lo_u32 v5, v3, v1
	v_add_u32_e32 v3, v5, v3
	v_cmp_ne_u32_e32 vcc, v4, v3
	s_waitcnt lgkmcnt(0)
	v_add_u32_e32 v16, -1, v1
	v_mul_lo_u32 v16, v16, v2
	s_and_saveexec_b64 s[4:5], vcc
	s_xor_b64 s[6:7], exec, s[4:5]
	s_cbranch_execz .LBB0_1552
	v_readlane_b32 s8, v253, 48
	v_readlane_b32 s9, v253, 49
	s_waitcnt lgkmcnt(0)
	s_nop 3
	s_add_u32 s8, s8, 0x3600
	s_addc_u32 s9, s9, 0
	s_mov_b32 s20, 0
	global_load_dword v2, v163, s[8:9] sc1
	s_sleep 10

; __device__ __forceinline__ unsigned xb_ld(unsigned* p)              { return __hip_atomic_load(p, __ATOMIC_RELAXED, __HIP_MEMORY_SCOPE_AGENT); }
; __device__ __forceinline__ unsigned xb_add(unsigned* p, unsigned v) { return __hip_atomic_fetch_add(p, v, __ATOMIC_RELAXED, __HIP_MEMORY_SCOPE_AGENT); }
; #define XB_SPIN(cond, bar) do { unsigned _sp = 0; while (cond) { __builtin_amdgcn_s_sleep(1); \
;     if ((++_sp & 255u) == 0u) { if (xb_ld(&(bar)[XB_TMO])) break; if (_sp > XB_SPIN_CAP) { atomicAdd(&(bar)[XB_TMO], 1u); break; } } } } while (0)
; __device__ __forceinline__ void xcd_barrier(const XcdBarrier& b) {
;     ...
;         if (old + 1u == (gen + 1u) * nloc) {
;             __builtin_amdgcn_fence(__ATOMIC_RELEASE, "agent");
;             asm volatile("s_waitcnt vmcnt(0)" ::: "memory");
;             const unsigned og = xb_add(&bar[XB_TOP], 1u);
;             const unsigned tg = og / nx;
;             if (og + 1u == (tg + 1u) * nx) xb_add(&bar[XB_TOPGEN], 1u);
;             else XB_SPIN(xb_ld(&bar[XB_TOPGEN]) == tg, bar);
;             __builtin_amdgcn_fence(__ATOMIC_ACQUIRE, "agent");
;             xb_add(&bar[XB_XGEN(b.x)], 1u);
;             asm volatile("s_waitcnt vmcnt(0)" ::: "memory");
;         } else {
;             XB_SPIN(xb_ld(&bar[XB_XGEN(b.x)]) == gen, bar);
;             __builtin_amdgcn_fence(__ATOMIC_ACQUIRE, "agent");
;             asm volatile("s_waitcnt vmcnt(0)" ::: "memory");
.Lbar_nl_done_0:
	s_waitcnt vmcnt(0)
.LBB0_1552:
	s_andn2_saveexec_b64 s[4:5], s[6:7]
	s_cbranch_execnz .LBB0_1553
	s_getpc_b64 s[98:99]
